# baseline (speedup 1.0000x reference)
_Z7k_finalPKfS0_S0_Pf:
	s_load_dwordx8 s[4:11], s[0:1], 0x0
	s_lshl_b32 s2, s2, 4
	v_lshrrev_b32_e32 v1, 3, v0
	v_or_b32_e32 v34, s2, v1
	v_bfe_u32 v1, v0, 2, 1
	s_ashr_i32 s0, s2, 3
	v_bfe_u32 v35, v0, 1, 1
	s_and_b32 s0, s0, -4
	v_lshlrev_b32_e32 v2, 1, v1
	v_lshlrev_b32_e32 v3, 4, v34
	v_and_b32_e32 v50, 1, v0
	v_or3_b32 v2, s0, v2, v35
	v_and_b32_e32 v3, 0x1f0, v3
	v_lshl_or_b32 v36, v50, 9, v3
	v_mov_b32_e32 v37, 0
	v_ashrrev_i32_e32 v3, 31, v2
	s_waitcnt lgkmcnt(0)
	v_lshl_add_u64 v[4:5], s[4:5], 0, v[36:37]
	v_lshlrev_b64 v[2:3], 10, v[2:3]
	v_lshl_add_u64 v[30:31], v[4:5], 0, v[2:3]
	s_mov_b32 s0, 0x80000
	v_add_co_u32_e32 v6, vcc, s0, v30
	s_mov_b32 s0, 0x100000
	s_nop 0
	v_addc_co_u32_e32 v7, vcc, 0, v31, vcc
	v_add_co_u32_e32 v14, vcc, s0, v30
	s_mov_b32 s0, 0x180000
	s_nop 0
	v_addc_co_u32_e32 v15, vcc, 0, v31, vcc
	v_add_co_u32_e32 v16, vcc, s0, v30
	s_mov_b32 s0, 0x200000
	s_nop 0
	v_addc_co_u32_e32 v17, vcc, 0, v31, vcc
	global_load_dwordx4 v[22:25], v[30:31], off
	global_load_dwordx4 v[2:5], v[6:7], off
	global_load_dwordx4 v[10:13], v[14:15], off
	s_nop 0
	global_load_dwordx4 v[6:9], v[16:17], off
	v_add_co_u32_e32 v26, vcc, s0, v30
	s_mov_b32 s0, 0x280000
	s_nop 0
	v_addc_co_u32_e32 v27, vcc, 0, v31, vcc
	v_add_co_u32_e32 v28, vcc, s0, v30
	s_mov_b32 s0, 0x300000
	s_nop 0
	v_addc_co_u32_e32 v29, vcc, 0, v31, vcc
	global_load_dwordx4 v[18:21], v[26:27], off
	global_load_dwordx4 v[14:17], v[28:29], off
	v_add_co_u32_e32 v26, vcc, s0, v30
	s_mov_b32 s0, 0x380000
	s_nop 0
	v_addc_co_u32_e32 v27, vcc, 0, v31, vcc
	v_add_co_u32_e32 v30, vcc, s0, v30
	global_load_dwordx4 v[26:29], v[26:27], off
	s_nop 0
	v_addc_co_u32_e32 v31, vcc, 0, v31, vcc
	global_load_dwordx4 v[30:33], v[30:31], off
	v_lshlrev_b32_e32 v36, 6, v35
	v_and_or_b32 v44, v0, 15, s2
	v_mov_b32_e32 v45, v37
	v_mov_b32_e32 v49, v37
	v_lshl_or_b32 v1, v1, 7, v36
	v_add_u32_e32 v48, 0x6000, v44
	v_mov_b32_e32 v39, v37
	v_mov_b32_e32 v41, v37
	v_mov_b32_e32 v43, v37
	v_mov_b32_e32 v47, v37
	v_add_u32_e32 v38, 0x1000, v44
	v_add_u32_e32 v40, 0x2000, v44
	v_add_u32_e32 v42, 0x4000, v44
	v_add_u32_e32 v46, 0x5000, v44
	v_lshl_or_b32 v36, v50, 4, v1
	v_lshl_add_u64 v[50:51], v[44:45], 2, s[8:9]
	v_lshl_add_u64 v[48:49], v[48:49], 2, s[8:9]
	v_lshl_add_u64 v[52:53], v[38:39], 2, s[8:9]
	v_lshl_add_u64 v[54:55], v[40:41], 2, s[8:9]
	v_lshl_add_u64 v[56:57], v[42:43], 2, s[8:9]
	v_lshl_add_u64 v[46:47], v[46:47], 2, s[8:9]
	global_load_dword v40, v[50:51], off
	global_load_dword v42, v[52:53], off
	global_load_dword v38, v[54:55], off
	global_load_dword v41, v[56:57], off
	global_load_dword v43, v[46:47], off
	global_load_dword v39, v[48:49], off
	v_ashrrev_i32_e32 v35, 31, v34
	v_lshlrev_b64 v[62:63], 8, v[34:35]
	v_lshl_add_u64 v[62:63], s[6:7], 0, v[62:63]
	v_lshl_add_u64 v[62:63], v[62:63], 0, v[36:37]
	global_load_dwordx4 v[64:67], v[62:63], off
	global_load_dwordx4 v[68:71], v[62:63], off offset:32
	v_add_u32_e32 v72, 0x3000, v44
	v_mov_b32_e32 v73, 0
	v_lshl_add_u64 v[72:73], v[72:73], 2, s[8:9]
	global_load_dword v76, v[72:73], off
	v_add_u32_e32 v74, 0x7000, v44
	v_mov_b32_e32 v75, 0
	v_lshl_add_u64 v[74:75], v[74:75], 2, s[8:9]
	global_load_dword v77, v[74:75], off
	s_mov_b64 s[0:1], 0x8000
	s_waitcnt vmcnt(17)
	v_cvt_f32_f16_e32 v58, v22
	s_waitcnt vmcnt(15)
	v_cvt_f32_f16_e32 v48, v10
	v_cvt_f32_f16_sdwa v49, v10 dst_sel:DWORD dst_unused:UNUSED_PAD src0_sel:WORD_1
	s_waitcnt vmcnt(14)
	v_cvt_f32_f16_e32 v50, v6
	v_cvt_f32_f16_sdwa v51, v6 dst_sel:DWORD dst_unused:UNUSED_PAD src0_sel:WORD_1
	v_cvt_f32_f16_e32 v10, v11
	v_cvt_f32_f16_sdwa v11, v11 dst_sel:DWORD dst_unused:UNUSED_PAD src0_sel:WORD_1
	v_cvt_f32_f16_e32 v6, v7
	v_cvt_f32_f16_sdwa v7, v7 dst_sel:DWORD dst_unused:UNUSED_PAD src0_sel:WORD_1
	v_cvt_f32_f16_sdwa v59, v22 dst_sel:DWORD dst_unused:UNUSED_PAD src0_sel:WORD_1
	v_cvt_f32_f16_e32 v60, v2
	v_cvt_f32_f16_sdwa v61, v2 dst_sel:DWORD dst_unused:UNUSED_PAD src0_sel:WORD_1
	v_cvt_f32_f16_e32 v22, v23
	v_cvt_f32_f16_sdwa v23, v23 dst_sel:DWORD dst_unused:UNUSED_PAD src0_sel:WORD_1
	v_cvt_f32_f16_e32 v2, v3
	v_cvt_f32_f16_sdwa v3, v3 dst_sel:DWORD dst_unused:UNUSED_PAD src0_sel:WORD_1
	s_waitcnt vmcnt(12)
	v_cvt_f32_f16_e32 v54, v14
	v_cvt_f32_f16_sdwa v55, v14 dst_sel:DWORD dst_unused:UNUSED_PAD src0_sel:WORD_1
	v_pk_add_f32 v[6:7], v[10:11], v[6:7]
	v_cvt_f32_f16_e32 v10, v19
	v_cvt_f32_f16_sdwa v11, v19 dst_sel:DWORD dst_unused:UNUSED_PAD src0_sel:WORD_1
	v_cvt_f32_f16_e32 v14, v15
	v_cvt_f32_f16_sdwa v15, v15 dst_sel:DWORD dst_unused:UNUSED_PAD src0_sel:WORD_1
	v_pk_add_f32 v[2:3], v[22:23], v[2:3]
	v_pk_add_f32 v[46:47], v[58:59], v[60:61]
	v_cvt_f32_f16_e32 v52, v18
	v_cvt_f32_f16_sdwa v53, v18 dst_sel:DWORD dst_unused:UNUSED_PAD src0_sel:WORD_1
	s_waitcnt vmcnt(11)
	v_cvt_f32_f16_e32 v56, v26
	v_cvt_f32_f16_sdwa v57, v26 dst_sel:DWORD dst_unused:UNUSED_PAD src0_sel:WORD_1
	s_waitcnt vmcnt(10)
	v_cvt_f32_f16_e32 v58, v30
	v_cvt_f32_f16_sdwa v59, v30 dst_sel:DWORD dst_unused:UNUSED_PAD src0_sel:WORD_1
	v_pk_add_f32 v[2:3], v[2:3], v[6:7]
	v_pk_add_f32 v[6:7], v[10:11], v[14:15]
	v_cvt_f32_f16_e32 v10, v27
	v_cvt_f32_f16_sdwa v11, v27 dst_sel:DWORD dst_unused:UNUSED_PAD src0_sel:WORD_1
	v_cvt_f32_f16_e32 v14, v31
	v_cvt_f32_f16_sdwa v15, v31 dst_sel:DWORD dst_unused:UNUSED_PAD src0_sel:WORD_1
	v_pk_add_f32 v[48:49], v[48:49], v[50:51]
	v_pk_add_f32 v[50:51], v[56:57], v[58:59]
	v_pk_add_f32 v[46:47], v[46:47], v[48:49]
	v_pk_add_f32 v[48:49], v[52:53], v[54:55]
	v_pk_add_f32 v[10:11], v[10:11], v[14:15]
	v_pk_add_f32 v[48:49], v[48:49], v[50:51]
	v_pk_add_f32 v[6:7], v[6:7], v[10:11]
	v_add_u32_e32 v50, 0x3000, v44
	v_add_u32_e32 v22, 0x7000, v44
	v_pk_add_f32 v[44:45], v[46:47], v[48:49]
	v_pk_add_f32 v[46:47], v[2:3], v[6:7]
	v_cvt_f32_f16_e32 v6, v24
	v_cvt_f32_f16_sdwa v7, v24 dst_sel:DWORD dst_unused:UNUSED_PAD src0_sel:WORD_1
	v_cvt_f32_f16_e32 v10, v4
	v_cvt_f32_f16_sdwa v11, v4 dst_sel:DWORD dst_unused:UNUSED_PAD src0_sel:WORD_1
	v_cvt_f32_f16_e32 v14, v12
	v_cvt_f32_f16_sdwa v15, v12 dst_sel:DWORD dst_unused:UNUSED_PAD src0_sel:WORD_1
	v_cvt_f32_f16_e32 v26, v8
	v_cvt_f32_f16_sdwa v27, v8 dst_sel:DWORD dst_unused:UNUSED_PAD src0_sel:WORD_1
	v_pk_add_f32 v[6:7], v[6:7], v[10:11]
	v_mov_b32_e32 v51, v37
	v_lshl_add_u64 v[18:19], v[50:51], 2, s[8:9]
	v_pk_add_f32 v[10:11], v[14:15], v[26:27]
	v_cvt_f32_f16_e32 v14, v16
	v_pk_add_f32 v[10:11], v[6:7], v[10:11]
	v_cvt_f32_f16_e32 v6, v20
	v_cvt_f32_f16_sdwa v7, v20 dst_sel:DWORD dst_unused:UNUSED_PAD src0_sel:WORD_1
	v_cvt_f32_f16_sdwa v15, v16 dst_sel:DWORD dst_unused:UNUSED_PAD src0_sel:WORD_1
	v_mov_b32_e32 v23, v37
	v_lshl_add_u64 v[22:23], v[22:23], 2, s[8:9]
	v_lshlrev_b64 v[18:19], 8, v[34:35]
	v_pk_add_f32 v[14:15], v[6:7], v[14:15]
	v_lshl_add_u64 v[6:7], s[6:7], 0, v[18:19]
	v_cvt_f32_f16_e32 v26, v25
	v_cvt_f32_f16_sdwa v27, v25 dst_sel:DWORD dst_unused:UNUSED_PAD src0_sel:WORD_1
	v_cvt_f32_f16_e32 v22, v28
	v_cvt_f32_f16_sdwa v23, v28 dst_sel:DWORD dst_unused:UNUSED_PAD src0_sel:WORD_1
	v_cvt_f32_f16_e32 v24, v32
	v_cvt_f32_f16_sdwa v25, v32 dst_sel:DWORD dst_unused:UNUSED_PAD src0_sel:WORD_1
	v_lshl_add_u64 v[30:31], v[6:7], 0, v[36:37]
	v_cvt_f32_f16_e32 v48, v5
	v_cvt_f32_f16_sdwa v49, v5 dst_sel:DWORD dst_unused:UNUSED_PAD src0_sel:WORD_1
	v_pk_add_f32 v[22:23], v[22:23], v[24:25]
	v_cvt_f32_f16_e32 v12, v13
	v_pk_add_f32 v[14:15], v[14:15], v[22:23]
	v_cvt_f32_f16_sdwa v13, v13 dst_sel:DWORD dst_unused:UNUSED_PAD src0_sel:WORD_1
	v_cvt_f32_f16_e32 v8, v9
	v_cvt_f32_f16_sdwa v9, v9 dst_sel:DWORD dst_unused:UNUSED_PAD src0_sel:WORD_1
	v_pk_add_f32 v[10:11], v[10:11], v[14:15]
	v_pk_add_f32 v[14:15], v[26:27], v[48:49]
	v_cvt_f32_f16_e32 v20, v21
	v_cvt_f32_f16_sdwa v21, v21 dst_sel:DWORD dst_unused:UNUSED_PAD src0_sel:WORD_1
	v_cvt_f32_f16_e32 v16, v17
	v_cvt_f32_f16_sdwa v17, v17 dst_sel:DWORD dst_unused:UNUSED_PAD src0_sel:WORD_1
	v_cvt_f32_f16_e32 v26, v29
	v_cvt_f32_f16_sdwa v27, v29 dst_sel:DWORD dst_unused:UNUSED_PAD src0_sel:WORD_1
	v_cvt_f32_f16_e32 v28, v33
	v_cvt_f32_f16_sdwa v29, v33 dst_sel:DWORD dst_unused:UNUSED_PAD src0_sel:WORD_1
	v_pk_add_f32 v[8:9], v[12:13], v[8:9]
	v_pk_add_f32 v[12:13], v[20:21], v[16:17]
	v_pk_add_f32 v[8:9], v[14:15], v[8:9]
	v_pk_add_f32 v[14:15], v[26:27], v[28:29]
	v_and_b32_e32 v16, 7, v0
	v_pk_add_f32 v[12:13], v[12:13], v[14:15]
	s_waitcnt vmcnt(3)
	v_mul_f32_e32 v1, v65, v45
	v_fmac_f32_e32 v1, v64, v44
	v_mbcnt_lo_u32_b32 v4, -1, 0
	v_fmac_f32_e32 v1, v66, v46
	v_mbcnt_hi_u32_b32 v14, -1, v4
	v_fmac_f32_e32 v1, v67, v47
	v_and_b32_e32 v5, 64, v14
	s_waitcnt vmcnt(0)
	v_fmac_f32_e32 v1, v68, v10
	v_xor_b32_e32 v4, 1, v14
	v_add_u32_e32 v15, 64, v5
	v_pk_add_f32 v[12:13], v[8:9], v[12:13]
	v_fmac_f32_e32 v1, v69, v11
	v_cmp_lt_i32_e32 vcc, v4, v15
	v_fmac_f32_e32 v1, v70, v12
	v_fmac_f32_e32 v1, v71, v13
	v_lshl_add_u64 v[4:5], s[10:11], 0, v[18:19]
	v_lshl_add_u64 v[6:7], v[4:5], 0, v[36:37]
	v_add_f32_dpp v1, v1, v1 quad_perm:[1,0,3,2] row_mask:0xf bank_mask:0xf
	v_lshl_add_u64 v[8:9], v[6:7], 0, s[0:1]
	s_mov_b32 s0, 0x8000
	s_nop 0
	v_add_f32_dpp v1, v1, v1 quad_perm:[2,3,0,1] row_mask:0xf bank_mask:0xf
	v_add_co_u32_e32 v6, vcc, s0, v6
	s_nop 1
	v_addc_co_u32_e32 v7, vcc, 0, v7, vcc
	v_mov_b32_dpp v4, v1 row_shl:4 row_mask:0xf bank_mask:0xf
	v_cmp_eq_u32_e32 vcc, 0, v16
	global_store_dwordx4 v[6:7], v[44:47], off sc1
	global_store_dwordx4 v[8:9], v[10:13], off offset:32 sc1
	s_and_saveexec_b64 s[0:1], vcc
	s_cbranch_execnz .LBB1_3
	s_or_b64 exec, exec, s[0:1]
	v_cmp_gt_u32_e32 vcc, 16, v0
	s_and_saveexec_b64 s[0:1], vcc
	s_cbranch_execnz .LBB1_4

.LBB1_4:
	s_waitcnt lgkmcnt(0)
	v_pk_add_f32 v[4:5], v[40:41], v[42:43]
	v_pk_add_f32 v[2:3], v[38:39], v[76:77]
	v_or_b32_e32 v0, s2, v0
	v_pk_add_f32 v[2:3], v[4:5], v[2:3]
	v_mov_b32_e32 v1, 0
	v_add_f32_e32 v2, v2, v3
	v_lshl_add_u64 v[0:1], v[0:1], 2, s[10:11]
	global_store_dword v[0:1], v2, off sc1
	s_endpgm
	s_nop 0
	s_nop 0
	s_nop 0
	s_nop 0
	s_nop 0
	s_nop 0
	s_nop 0
	s_nop 0
	s_nop 0
	s_nop 0
	s_nop 0
	s_nop 0
	s_nop 0
	s_nop 0
	s_nop 0
	s_nop 0
	s_nop 0
	s_nop 0
	s_nop 0
	s_nop 0
	s_nop 0
	s_nop 0
	s_nop 0
	s_nop 0
	s_nop 0
	s_nop 0
	s_nop 0
	s_nop 0
	s_nop 0
	s_nop 0
	s_nop 0
	s_endpgm
